# SwiGLU epilogue of the fp8 up GEMM: packed v_pk_mul/v_pk_fma on adjacent accumulators (same IEEE ops), fp8 convert without the zero-fill moves
# speedup vs baseline: 1.0118x; 1.0118x over previous
; DI unsigned pk4_fp8(float a, float b, float c, float d) { unsigned p = 0u; p = __builtin_amdgcn_cvt_pk_fp8_f32(f8clamp(a), f8clamp(b), p, false); p = __builtin_amdgcn_cvt_pk_fp8_f32(f8clamp(c), f8clamp(d), p, true); return p; }
; DI float swiglu8(float xa, float xg) {
;     constexpr float sc = F8_HSC * F8_WSC, K1 = -1.4426950408889634f / sc, IK2 = sc * sc / F8_ASC;
;     const float e = __builtin_amdgcn_exp2f(xa * K1);
;     return (xa * xg) * __builtin_amdgcn_rcpf(__builtin_fmaf(e, IK2, IK2));
; }
;     DI void operator()(const pg8::f32x4 (&acc)[2][2][4][2], const pg8::Unit& u, int wr, int wc, int fr, int fq) const {
;         const int lpn = u.pn % nN; const int row0 = u.pm * 256 + wr * 64 + fr, col0 = lpn * 128 + wc * 32 + 8 * fq;
; #pragma unroll
;         for (int ai = 0; ai < 2; ++ai)
; #pragma unroll
;             for (int m = 0; m < 4; ++m) { unsigned char* p = act + (size_t)(row0 + ai * 128 + m * 16) * FF + col0;
;                 const pg8::f32x4 a0 = acc[ai][0][m][0], a1 = acc[ai][0][m][1], g0 = acc[ai][1][m][0], g1 = acc[ai][1][m][1];
;                 uint2 w; w.x = pk4_fp8(swiglu8(a0[0], g0[0]), swiglu8(a0[1], g0[1]), swiglu8(a0[2], g0[2]), swiglu8(a0[3], g0[3]));
;                 w.y = pk4_fp8(swiglu8(a1[0], g1[0]), swiglu8(a1[1], g1[1]), swiglu8(a1[2], g1[2]), swiglu8(a1[3], g1[3]));
;                 *(uint2*)p = w; }
;     }
.LBB0_1391:
	s_mov_b32 s84, 0xbb38aa3b
	s_mov_b32 s85, 0xbb38aa3b
	s_mov_b32 s86, 0x46800000
	s_mov_b32 s87, 0x46800000
	v_pk_mul_f32 v[134:135], v[134:135], v[126:127]
	v_pk_mul_f32 v[136:137], v[136:137], v[128:129]
	v_pk_mul_f32 v[130:131], v[130:131], v[122:123]
	v_pk_mul_f32 v[132:133], v[132:133], v[124:125]
	v_pk_mul_f32 v[126:127], v[126:127], s[84:85]
	v_pk_mul_f32 v[128:129], v[128:129], s[84:85]
	v_pk_mul_f32 v[122:123], v[122:123], s[84:85]
	v_pk_mul_f32 v[124:125], v[124:125], s[84:85]
	v_exp_f32_e32 v126, v126
	v_exp_f32_e32 v127, v127
	v_exp_f32_e32 v128, v128
	v_exp_f32_e32 v129, v129
	v_exp_f32_e32 v122, v122
	v_exp_f32_e32 v123, v123
	v_exp_f32_e32 v124, v124
	v_exp_f32_e32 v125, v125
	v_pk_fma_f32 v[126:127], v[126:127], s[86:87], v[172:173] op_sel:[0,0,1] op_sel_hi:[1,1,1]
	v_pk_fma_f32 v[128:129], v[128:129], s[86:87], v[172:173] op_sel:[0,0,1] op_sel_hi:[1,1,1]
	v_pk_fma_f32 v[122:123], v[122:123], s[86:87], v[172:173] op_sel:[0,0,1] op_sel_hi:[1,1,1]
	v_pk_fma_f32 v[124:125], v[124:125], s[86:87], v[172:173] op_sel:[0,0,1] op_sel_hi:[1,1,1]
	v_rcp_f32_e32 v126, v126
	v_rcp_f32_e32 v127, v127
	v_rcp_f32_e32 v128, v128
	v_rcp_f32_e32 v129, v129
	v_rcp_f32_e32 v122, v122
	v_rcp_f32_e32 v123, v123
	v_rcp_f32_e32 v124, v124
	v_rcp_f32_e32 v125, v125
	v_pk_mul_f32 v[134:135], v[134:135], v[126:127]
	v_pk_mul_f32 v[136:137], v[136:137], v[128:129]
	v_pk_mul_f32 v[130:131], v[130:131], v[122:123]
	v_pk_mul_f32 v[132:133], v[132:133], v[124:125]
	v_med3_f32 v134, v134, s64, v174
	v_med3_f32 v135, v135, s64, v174
	v_med3_f32 v136, v136, s64, v174
	v_med3_f32 v137, v137, s64, v174
	v_med3_f32 v130, v130, s64, v174
	v_med3_f32 v131, v131, s64, v174
	v_med3_f32 v132, v132, s64, v174
	v_med3_f32 v133, v133, s64, v174
	v_cvt_pk_fp8_f32 v126, v134, v135
	v_cvt_pk_fp8_f32 v126, v136, v137 op_sel:[0,0,1]
	v_cvt_pk_fp8_f32 v127, v130, v131
	v_cvt_pk_fp8_f32 v127, v132, v133 op_sel:[0,0,1]
	s_mul_hi_i32 s5, s72, 0x2e8ba2e9
	s_lshr_b32 s6, s5, 31
	s_lshr_b32 s5, s5, 2
	s_add_i32 s5, s5, s6
	s_mul_i32 s5, s5, 22
	s_sub_i32 s5, s72, s5
	v_lshl_add_u32 v6, s71, 8, v168
	v_lshl_or_b32 v2, s5, 7, v171
	v_mov_b64_e32 v[4:5], s[16:17]
	v_ashrrev_i32_e32 v3, 31, v2
	v_mad_i64_i32 v[122:123], s[6:7], v6, s51, v[4:5]
	v_lshl_add_u64 v[122:123], v[122:123], 0, v[2:3]
	global_store_dwordx2 v[122:123], v[126:127], off
	v_pk_mul_f32 v[118:119], v[118:119], v[110:111]
	v_pk_mul_f32 v[120:121], v[120:121], v[112:113]
	v_pk_mul_f32 v[114:115], v[114:115], v[106:107]
	v_pk_mul_f32 v[116:117], v[116:117], v[108:109]
	v_pk_mul_f32 v[110:111], v[110:111], s[84:85]
	v_pk_mul_f32 v[112:113], v[112:113], s[84:85]
	v_pk_mul_f32 v[106:107], v[106:107], s[84:85]
	v_pk_mul_f32 v[108:109], v[108:109], s[84:85]
	v_exp_f32_e32 v110, v110
	v_exp_f32_e32 v111, v111
	v_exp_f32_e32 v112, v112
	v_exp_f32_e32 v113, v113
	v_exp_f32_e32 v106, v106
	v_exp_f32_e32 v107, v107
	v_exp_f32_e32 v108, v108
	v_exp_f32_e32 v109, v109
	v_pk_fma_f32 v[110:111], v[110:111], s[86:87], v[172:173] op_sel:[0,0,1] op_sel_hi:[1,1,1]
	v_pk_fma_f32 v[112:113], v[112:113], s[86:87], v[172:173] op_sel:[0,0,1] op_sel_hi:[1,1,1]
	v_pk_fma_f32 v[106:107], v[106:107], s[86:87], v[172:173] op_sel:[0,0,1] op_sel_hi:[1,1,1]
	v_pk_fma_f32 v[108:109], v[108:109], s[86:87], v[172:173] op_sel:[0,0,1] op_sel_hi:[1,1,1]
	v_rcp_f32_e32 v110, v110
	v_rcp_f32_e32 v111, v111
	v_rcp_f32_e32 v112, v112
	v_rcp_f32_e32 v113, v113
	v_rcp_f32_e32 v106, v106
	v_rcp_f32_e32 v107, v107
	v_rcp_f32_e32 v108, v108
	v_rcp_f32_e32 v109, v109
	v_pk_mul_f32 v[118:119], v[118:119], v[110:111]
	v_pk_mul_f32 v[120:121], v[120:121], v[112:113]
	v_pk_mul_f32 v[114:115], v[114:115], v[106:107]
	v_pk_mul_f32 v[116:117], v[116:117], v[108:109]
	v_med3_f32 v118, v118, s64, v174
	v_med3_f32 v119, v119, s64, v174
	v_med3_f32 v120, v120, s64, v174
	v_med3_f32 v121, v121, s64, v174
	v_med3_f32 v114, v114, s64, v174
	v_med3_f32 v115, v115, s64, v174
	v_med3_f32 v116, v116, s64, v174
	v_med3_f32 v117, v117, s64, v174
	v_cvt_pk_fp8_f32 v110, v118, v119
	v_cvt_pk_fp8_f32 v110, v120, v121 op_sel:[0,0,1]
	v_cvt_pk_fp8_f32 v111, v114, v115
	v_cvt_pk_fp8_f32 v111, v116, v117 op_sel:[0,0,1]
	v_or_b32_e32 v7, 16, v6
	v_mad_i64_i32 v[106:107], s[6:7], v7, s51, v[4:5]
	v_lshl_add_u64 v[106:107], v[106:107], 0, v[2:3]
	global_store_dwordx2 v[106:107], v[110:111], off
	v_pk_mul_f32 v[102:103], v[102:103], v[94:95]
	v_pk_mul_f32 v[104:105], v[104:105], v[96:97]
	v_pk_mul_f32 v[98:99], v[98:99], v[90:91]
	v_pk_mul_f32 v[100:101], v[100:101], v[92:93]
	v_pk_mul_f32 v[94:95], v[94:95], s[84:85]
	v_pk_mul_f32 v[96:97], v[96:97], s[84:85]
	v_pk_mul_f32 v[90:91], v[90:91], s[84:85]
	v_pk_mul_f32 v[92:93], v[92:93], s[84:85]
	v_exp_f32_e32 v94, v94
	v_exp_f32_e32 v95, v95
	v_exp_f32_e32 v96, v96
	v_exp_f32_e32 v97, v97
	v_exp_f32_e32 v90, v90
	v_exp_f32_e32 v91, v91
	v_exp_f32_e32 v92, v92
	v_exp_f32_e32 v93, v93
	v_pk_fma_f32 v[94:95], v[94:95], s[86:87], v[172:173] op_sel:[0,0,1] op_sel_hi:[1,1,1]
	v_pk_fma_f32 v[96:97], v[96:97], s[86:87], v[172:173] op_sel:[0,0,1] op_sel_hi:[1,1,1]
	v_pk_fma_f32 v[90:91], v[90:91], s[86:87], v[172:173] op_sel:[0,0,1] op_sel_hi:[1,1,1]
	v_pk_fma_f32 v[92:93], v[92:93], s[86:87], v[172:173] op_sel:[0,0,1] op_sel_hi:[1,1,1]
	v_rcp_f32_e32 v94, v94
	v_rcp_f32_e32 v95, v95
	v_rcp_f32_e32 v96, v96
	v_rcp_f32_e32 v97, v97
	v_rcp_f32_e32 v90, v90
	v_rcp_f32_e32 v91, v91
	v_rcp_f32_e32 v92, v92
	v_rcp_f32_e32 v93, v93
	v_pk_mul_f32 v[102:103], v[102:103], v[94:95]
	v_pk_mul_f32 v[104:105], v[104:105], v[96:97]
	v_pk_mul_f32 v[98:99], v[98:99], v[90:91]
	v_pk_mul_f32 v[100:101], v[100:101], v[92:93]
	v_med3_f32 v102, v102, s64, v174
; DI unsigned pk4_fp8(float a, float b, float c, float d) { unsigned p = 0u; p = __builtin_amdgcn_cvt_pk_fp8_f32(f8clamp(a), f8clamp(b), p, false); p = __builtin_amdgcn_cvt_pk_fp8_f32(f8clamp(c), f8clamp(d), p, true); return p; }
; DI float swiglu8(float xa, float xg) {
;     constexpr float sc = F8_HSC * F8_WSC, K1 = -1.4426950408889634f / sc, IK2 = sc * sc / F8_ASC;
;     const float e = __builtin_amdgcn_exp2f(xa * K1);
;     return (xa * xg) * __builtin_amdgcn_rcpf(__builtin_fmaf(e, IK2, IK2));
; }
;     DI void operator()(const pg8::f32x4 (&acc)[2][2][4][2], const pg8::Unit& u, int wr, int wc, int fr, int fq) const {
;         const int lpn = u.pn % nN; const int row0 = u.pm * 256 + wr * 64 + fr, col0 = lpn * 128 + wc * 32 + 8 * fq;
; #pragma unroll
;         for (int ai = 0; ai < 2; ++ai)
; #pragma unroll
;             for (int m = 0; m < 4; ++m) { unsigned char* p = act + (size_t)(row0 + ai * 128 + m * 16) * FF + col0;
;                 const pg8::f32x4 a0 = acc[ai][0][m][0], a1 = acc[ai][0][m][1], g0 = acc[ai][1][m][0], g1 = acc[ai][1][m][1];
;                 uint2 w; w.x = pk4_fp8(swiglu8(a0[0], g0[0]), swiglu8(a0[1], g0[1]), swiglu8(a0[2], g0[2]), swiglu8(a0[3], g0[3]));
;                 w.y = pk4_fp8(swiglu8(a1[0], g1[0]), swiglu8(a1[1], g1[1]), swiglu8(a1[2], g1[2]), swiglu8(a1[3], g1[3]));
;                 *(uint2*)p = w; }
;     }
	v_med3_f32 v103, v103, s64, v174
	v_med3_f32 v104, v104, s64, v174
	v_med3_f32 v105, v105, s64, v174
	v_med3_f32 v98, v98, s64, v174
	v_med3_f32 v99, v99, s64, v174
	v_med3_f32 v100, v100, s64, v174
	v_med3_f32 v101, v101, s64, v174
	v_cvt_pk_fp8_f32 v94, v102, v103
	v_cvt_pk_fp8_f32 v94, v104, v105 op_sel:[0,0,1]
	v_cvt_pk_fp8_f32 v95, v98, v99
	v_cvt_pk_fp8_f32 v95, v100, v101 op_sel:[0,0,1]
	v_or_b32_e32 v7, 32, v6
	v_mad_i64_i32 v[90:91], s[6:7], v7, s51, v[4:5]
	v_lshl_add_u64 v[90:91], v[90:91], 0, v[2:3]
	global_store_dwordx2 v[90:91], v[94:95], off
	v_pk_mul_f32 v[86:87], v[86:87], v[78:79]
	v_pk_mul_f32 v[88:89], v[88:89], v[80:81]
	v_pk_mul_f32 v[82:83], v[82:83], v[70:71]
	v_pk_mul_f32 v[84:85], v[84:85], v[72:73]
	v_pk_mul_f32 v[78:79], v[78:79], s[84:85]
	v_pk_mul_f32 v[80:81], v[80:81], s[84:85]
	v_pk_mul_f32 v[70:71], v[70:71], s[84:85]
	v_pk_mul_f32 v[72:73], v[72:73], s[84:85]
	v_exp_f32_e32 v78, v78
	v_exp_f32_e32 v79, v79
	v_exp_f32_e32 v80, v80
	v_exp_f32_e32 v81, v81
	v_exp_f32_e32 v70, v70
	v_exp_f32_e32 v71, v71
	v_exp_f32_e32 v72, v72
	v_exp_f32_e32 v73, v73
	v_pk_fma_f32 v[78:79], v[78:79], s[86:87], v[172:173] op_sel:[0,0,1] op_sel_hi:[1,1,1]
	v_pk_fma_f32 v[80:81], v[80:81], s[86:87], v[172:173] op_sel:[0,0,1] op_sel_hi:[1,1,1]
	v_pk_fma_f32 v[70:71], v[70:71], s[86:87], v[172:173] op_sel:[0,0,1] op_sel_hi:[1,1,1]
	v_pk_fma_f32 v[72:73], v[72:73], s[86:87], v[172:173] op_sel:[0,0,1] op_sel_hi:[1,1,1]
	v_rcp_f32_e32 v78, v78
	v_rcp_f32_e32 v79, v79
	v_rcp_f32_e32 v80, v80
	v_rcp_f32_e32 v81, v81
	v_rcp_f32_e32 v70, v70
	v_rcp_f32_e32 v71, v71
	v_rcp_f32_e32 v72, v72
	v_rcp_f32_e32 v73, v73
	v_pk_mul_f32 v[86:87], v[86:87], v[78:79]
	v_pk_mul_f32 v[88:89], v[88:89], v[80:81]
	v_pk_mul_f32 v[82:83], v[82:83], v[70:71]
	v_pk_mul_f32 v[84:85], v[84:85], v[72:73]
	v_med3_f32 v86, v86, s64, v174
	v_med3_f32 v87, v87, s64, v174
	v_med3_f32 v88, v88, s64, v174
	v_med3_f32 v89, v89, s64, v174
	v_med3_f32 v82, v82, s64, v174
	v_med3_f32 v83, v83, s64, v174
	v_med3_f32 v84, v84, s64, v174
	v_med3_f32 v85, v85, s64, v174
	v_cvt_pk_fp8_f32 v78, v86, v87
	v_cvt_pk_fp8_f32 v78, v88, v89 op_sel:[0,0,1]
	v_cvt_pk_fp8_f32 v79, v82, v83
	v_cvt_pk_fp8_f32 v79, v84, v85 op_sel:[0,0,1]
	v_or_b32_e32 v7, 48, v6
	v_mad_i64_i32 v[70:71], s[6:7], v7, s51, v[4:5]
	v_lshl_add_u64 v[70:71], v[70:71], 0, v[2:3]
	global_store_dwordx2 v[70:71], v[78:79], off
	v_pk_mul_f32 v[74:75], v[74:75], v[62:63]
	v_pk_mul_f32 v[76:77], v[76:77], v[64:65]
	v_pk_mul_f32 v[66:67], v[66:67], v[58:59]
	v_pk_mul_f32 v[68:69], v[68:69], v[60:61]
	v_pk_mul_f32 v[62:63], v[62:63], s[84:85]
	v_pk_mul_f32 v[64:65], v[64:65], s[84:85]
	v_pk_mul_f32 v[58:59], v[58:59], s[84:85]
	v_pk_mul_f32 v[60:61], v[60:61], s[84:85]
	v_exp_f32_e32 v62, v62
	v_exp_f32_e32 v63, v63
	v_exp_f32_e32 v64, v64
	v_exp_f32_e32 v65, v65
	v_exp_f32_e32 v58, v58
	v_exp_f32_e32 v59, v59
	v_exp_f32_e32 v60, v60
	v_exp_f32_e32 v61, v61
	v_pk_fma_f32 v[62:63], v[62:63], s[86:87], v[172:173] op_sel:[0,0,1] op_sel_hi:[1,1,1]
	v_pk_fma_f32 v[64:65], v[64:65], s[86:87], v[172:173] op_sel:[0,0,1] op_sel_hi:[1,1,1]
	v_pk_fma_f32 v[58:59], v[58:59], s[86:87], v[172:173] op_sel:[0,0,1] op_sel_hi:[1,1,1]
	v_pk_fma_f32 v[60:61], v[60:61], s[86:87], v[172:173] op_sel:[0,0,1] op_sel_hi:[1,1,1]
	v_rcp_f32_e32 v62, v62
	v_rcp_f32_e32 v63, v63
	v_rcp_f32_e32 v64, v64
	v_rcp_f32_e32 v65, v65
	v_rcp_f32_e32 v58, v58
	v_rcp_f32_e32 v59, v59
	v_rcp_f32_e32 v60, v60
	v_rcp_f32_e32 v61, v61
	v_pk_mul_f32 v[74:75], v[74:75], v[62:63]
	v_pk_mul_f32 v[76:77], v[76:77], v[64:65]
	v_pk_mul_f32 v[66:67], v[66:67], v[58:59]
	v_pk_mul_f32 v[68:69], v[68:69], v[60:61]
	v_med3_f32 v74, v74, s64, v174
	v_med3_f32 v75, v75, s64, v174
	v_med3_f32 v76, v76, s64, v174
	v_med3_f32 v77, v77, s64, v174
	v_med3_f32 v66, v66, s64, v174
	v_med3_f32 v67, v67, s64, v174
	v_med3_f32 v68, v68, s64, v174
	v_med3_f32 v69, v69, s64, v174
	v_cvt_pk_fp8_f32 v62, v74, v75
	v_cvt_pk_fp8_f32 v62, v76, v77 op_sel:[0,0,1]
	v_cvt_pk_fp8_f32 v63, v66, v67
	v_cvt_pk_fp8_f32 v63, v68, v69 op_sel:[0,0,1]
	v_add_u32_e32 v7, 0x80, v6
	v_mad_i64_i32 v[58:59], s[6:7], v7, s51, v[4:5]
	v_lshl_add_u64 v[58:59], v[58:59], 0, v[2:3]
	global_store_dwordx2 v[58:59], v[62:63], off
	v_pk_mul_f32 v[54:55], v[54:55], v[46:47]
	v_pk_mul_f32 v[56:57], v[56:57], v[48:49]
	v_pk_mul_f32 v[50:51], v[50:51], v[42:43]
	v_pk_mul_f32 v[52:53], v[52:53], v[44:45]
	v_pk_mul_f32 v[46:47], v[46:47], s[84:85]
	v_pk_mul_f32 v[48:49], v[48:49], s[84:85]
	v_pk_mul_f32 v[42:43], v[42:43], s[84:85]
	v_pk_mul_f32 v[44:45], v[44:45], s[84:85]
	v_exp_f32_e32 v46, v46
	v_exp_f32_e32 v47, v47
	v_exp_f32_e32 v48, v48
	v_exp_f32_e32 v49, v49
	v_exp_f32_e32 v42, v42
	v_exp_f32_e32 v43, v43
	v_exp_f32_e32 v44, v44
	v_exp_f32_e32 v45, v45
	v_pk_fma_f32 v[46:47], v[46:47], s[86:87], v[172:173] op_sel:[0,0,1] op_sel_hi:[1,1,1]
	v_pk_fma_f32 v[48:49], v[48:49], s[86:87], v[172:173] op_sel:[0,0,1] op_sel_hi:[1,1,1]
	v_pk_fma_f32 v[42:43], v[42:43], s[86:87], v[172:173] op_sel:[0,0,1] op_sel_hi:[1,1,1]
	v_pk_fma_f32 v[44:45], v[44:45], s[86:87], v[172:173] op_sel:[0,0,1] op_sel_hi:[1,1,1]
	v_rcp_f32_e32 v46, v46
	v_rcp_f32_e32 v47, v47
	v_rcp_f32_e32 v48, v48
	v_rcp_f32_e32 v49, v49
	v_rcp_f32_e32 v42, v42
	v_rcp_f32_e32 v43, v43
	v_rcp_f32_e32 v44, v44
	v_rcp_f32_e32 v45, v45
	v_pk_mul_f32 v[54:55], v[54:55], v[46:47]
	v_pk_mul_f32 v[56:57], v[56:57], v[48:49]
	v_pk_mul_f32 v[50:51], v[50:51], v[42:43]
	v_pk_mul_f32 v[52:53], v[52:53], v[44:45]
	v_med3_f32 v54, v54, s64, v174
	v_med3_f32 v55, v55, s64, v174
	v_med3_f32 v56, v56, s64, v174
	v_med3_f32 v57, v57, s64, v174
	v_med3_f32 v50, v50, s64, v174
; DI unsigned pk4_fp8(float a, float b, float c, float d) { unsigned p = 0u; p = __builtin_amdgcn_cvt_pk_fp8_f32(f8clamp(a), f8clamp(b), p, false); p = __builtin_amdgcn_cvt_pk_fp8_f32(f8clamp(c), f8clamp(d), p, true); return p; }
; template <class Epi, class Sched, bool ALIGN_EPI = false, bool SP2 = false, bool F8 = false>
; __device__ __forceinline__ void gemm_phase(PG8_LAS unsigned char* lds, const Gemm g, const Sched& S, const Epi& E) {
;     ...
; #pragma unroll
;         for (int a = 0; a < 2; ++a)
; #pragma unroll
;             for (int b = 0; b < 2; ++b)
; #pragma unroll
;                 for (int m = 0; m < 4; ++m)
; #pragma unroll
;                     for (int n = 0; n < 2; ++n) { acc[a][b][m][n] = (f32x4){0.f, 0.f, 0.f, 0.f}; if constexpr (F8) asm volatile("" : "+v"(acc[a][b][m][n])); }
; DI float swiglu8(float xa, float xg) {
;     constexpr float sc = F8_HSC * F8_WSC, K1 = -1.4426950408889634f / sc, IK2 = sc * sc / F8_ASC;
;     const float e = __builtin_amdgcn_exp2f(xa * K1);
;     return (xa * xg) * __builtin_amdgcn_rcpf(__builtin_fmaf(e, IK2, IK2));
; }
;     DI void operator()(const pg8::f32x4 (&acc)[2][2][4][2], const pg8::Unit& u, int wr, int wc, int fr, int fq) const {
;         const int lpn = u.pn % nN; const int row0 = u.pm * 256 + wr * 64 + fr, col0 = lpn * 128 + wc * 32 + 8 * fq;
; #pragma unroll
;         for (int ai = 0; ai < 2; ++ai)
; #pragma unroll
;             for (int m = 0; m < 4; ++m) { unsigned char* p = act + (size_t)(row0 + ai * 128 + m * 16) * FF + col0;
;                 const pg8::f32x4 a0 = acc[ai][0][m][0], a1 = acc[ai][0][m][1], g0 = acc[ai][1][m][0], g1 = acc[ai][1][m][1];
;                 uint2 w; w.x = pk4_fp8(swiglu8(a0[0], g0[0]), swiglu8(a0[1], g0[1]), swiglu8(a0[2], g0[2]), swiglu8(a0[3], g0[3]));
;                 w.y = pk4_fp8(swiglu8(a1[0], g1[0]), swiglu8(a1[1], g1[1]), swiglu8(a1[2], g1[2]), swiglu8(a1[3], g1[3]));
;                 *(uint2*)p = w; }
;     }
	v_med3_f32 v51, v51, s64, v174
	v_med3_f32 v52, v52, s64, v174
	v_med3_f32 v53, v53, s64, v174
	v_cvt_pk_fp8_f32 v46, v54, v55
	v_cvt_pk_fp8_f32 v46, v56, v57 op_sel:[0,0,1]
	v_cvt_pk_fp8_f32 v47, v50, v51
	v_cvt_pk_fp8_f32 v47, v52, v53 op_sel:[0,0,1]
	v_add_u32_e32 v7, 0x90, v6
	v_mad_i64_i32 v[42:43], s[6:7], v7, s51, v[4:5]
	v_lshl_add_u64 v[42:43], v[42:43], 0, v[2:3]
	global_store_dwordx2 v[42:43], v[46:47], off
	v_pk_mul_f32 v[38:39], v[38:39], v[30:31]
	v_pk_mul_f32 v[40:41], v[40:41], v[32:33]
	v_pk_mul_f32 v[34:35], v[34:35], v[26:27]
	v_pk_mul_f32 v[36:37], v[36:37], v[28:29]
	v_pk_mul_f32 v[30:31], v[30:31], s[84:85]
	v_pk_mul_f32 v[32:33], v[32:33], s[84:85]
	v_pk_mul_f32 v[26:27], v[26:27], s[84:85]
	v_pk_mul_f32 v[28:29], v[28:29], s[84:85]
	v_exp_f32_e32 v30, v30
	v_exp_f32_e32 v31, v31
	v_exp_f32_e32 v32, v32
	v_exp_f32_e32 v33, v33
	v_exp_f32_e32 v26, v26
	v_exp_f32_e32 v27, v27
	v_exp_f32_e32 v28, v28
	v_exp_f32_e32 v29, v29
	v_pk_fma_f32 v[30:31], v[30:31], s[86:87], v[172:173] op_sel:[0,0,1] op_sel_hi:[1,1,1]
	v_pk_fma_f32 v[32:33], v[32:33], s[86:87], v[172:173] op_sel:[0,0,1] op_sel_hi:[1,1,1]
	v_pk_fma_f32 v[26:27], v[26:27], s[86:87], v[172:173] op_sel:[0,0,1] op_sel_hi:[1,1,1]
	v_pk_fma_f32 v[28:29], v[28:29], s[86:87], v[172:173] op_sel:[0,0,1] op_sel_hi:[1,1,1]
	v_rcp_f32_e32 v30, v30
	v_rcp_f32_e32 v31, v31
	v_rcp_f32_e32 v32, v32
	v_rcp_f32_e32 v33, v33
	v_rcp_f32_e32 v26, v26
	v_rcp_f32_e32 v27, v27
	v_rcp_f32_e32 v28, v28
	v_rcp_f32_e32 v29, v29
	v_pk_mul_f32 v[38:39], v[38:39], v[30:31]
	v_pk_mul_f32 v[40:41], v[40:41], v[32:33]
	v_pk_mul_f32 v[34:35], v[34:35], v[26:27]
	v_pk_mul_f32 v[36:37], v[36:37], v[28:29]
	v_med3_f32 v38, v38, s64, v174
	v_med3_f32 v39, v39, s64, v174
	v_med3_f32 v40, v40, s64, v174
	v_med3_f32 v41, v41, s64, v174
	v_med3_f32 v34, v34, s64, v174
	v_med3_f32 v35, v35, s64, v174
	v_med3_f32 v36, v36, s64, v174
	v_med3_f32 v37, v37, s64, v174
	v_cvt_pk_fp8_f32 v30, v38, v39
	v_cvt_pk_fp8_f32 v30, v40, v41 op_sel:[0,0,1]
	v_cvt_pk_fp8_f32 v31, v34, v35
	v_cvt_pk_fp8_f32 v31, v36, v37 op_sel:[0,0,1]
	v_add_u32_e32 v7, 0xa0, v6
	v_mad_i64_i32 v[26:27], s[6:7], v7, s51, v[4:5]
	v_lshl_add_u64 v[26:27], v[26:27], 0, v[2:3]
	global_store_dwordx2 v[26:27], v[30:31], off
	v_pk_mul_f32 v[22:23], v[22:23], v[18:19]
	v_pk_mul_f32 v[24:25], v[24:25], v[20:21]
	v_pk_mul_f32 v[10:11], v[10:11], v[14:15]
	v_pk_mul_f32 v[12:13], v[12:13], v[16:17]
	v_pk_mul_f32 v[18:19], v[18:19], s[84:85]
	v_pk_mul_f32 v[20:21], v[20:21], s[84:85]
	v_pk_mul_f32 v[14:15], v[14:15], s[84:85]
	v_pk_mul_f32 v[16:17], v[16:17], s[84:85]
	v_exp_f32_e32 v18, v18
	v_exp_f32_e32 v19, v19
	v_exp_f32_e32 v20, v20
	v_exp_f32_e32 v21, v21
	v_exp_f32_e32 v14, v14
	v_exp_f32_e32 v15, v15
	v_exp_f32_e32 v16, v16
	v_exp_f32_e32 v17, v17
	v_pk_fma_f32 v[18:19], v[18:19], s[86:87], v[172:173] op_sel:[0,0,1] op_sel_hi:[1,1,1]
	v_pk_fma_f32 v[20:21], v[20:21], s[86:87], v[172:173] op_sel:[0,0,1] op_sel_hi:[1,1,1]
	v_pk_fma_f32 v[14:15], v[14:15], s[86:87], v[172:173] op_sel:[0,0,1] op_sel_hi:[1,1,1]
	v_pk_fma_f32 v[16:17], v[16:17], s[86:87], v[172:173] op_sel:[0,0,1] op_sel_hi:[1,1,1]
	v_rcp_f32_e32 v18, v18
	v_rcp_f32_e32 v19, v19
	v_rcp_f32_e32 v20, v20
	v_rcp_f32_e32 v21, v21
	v_rcp_f32_e32 v14, v14
	v_rcp_f32_e32 v15, v15
	v_rcp_f32_e32 v16, v16
	v_rcp_f32_e32 v17, v17
	v_pk_mul_f32 v[22:23], v[22:23], v[18:19]
	v_pk_mul_f32 v[24:25], v[24:25], v[20:21]
	v_pk_mul_f32 v[10:11], v[10:11], v[14:15]
	v_pk_mul_f32 v[12:13], v[12:13], v[16:17]
	v_med3_f32 v22, v22, s64, v174
	v_med3_f32 v23, v23, s64, v174
	v_med3_f32 v24, v24, s64, v174
	v_med3_f32 v25, v25, s64, v174
	v_med3_f32 v10, v10, s64, v174
	v_med3_f32 v11, v11, s64, v174
	v_med3_f32 v12, v12, s64, v174
	v_med3_f32 v13, v13, s64, v174
	v_cvt_pk_fp8_f32 v18, v22, v23
	v_cvt_pk_fp8_f32 v18, v24, v25 op_sel:[0,0,1]
	v_cvt_pk_fp8_f32 v19, v10, v11
	v_cvt_pk_fp8_f32 v19, v12, v13 op_sel:[0,0,1]
	v_add_u32_e32 v8, 0xb0, v6
	v_mad_i64_i32 v[4:5], s[6:7], v8, s51, v[4:5]
	v_lshl_add_u64 v[2:3], v[4:5], 0, v[2:3]
	s_and_b64 vcc, exec, s[2:3]
	s_mov_b64 s[2:3], -1
	global_store_dwordx2 v[2:3], v[18:19], off
	s_cbranch_vccnz .LBB0_1379
	s_mov_b32 s6, s4
	s_mov_b32 s7, s4
	s_mov_b32 s5, s4
	v_mov_b64_e32 v[12:13], s[6:7]
	v_mov_b64_e32 v[128:129], s[6:7]
	v_mov_b64_e32 v[124:125], s[6:7]
	v_mov_b64_e32 v[112:113], s[6:7]
	v_mov_b64_e32 v[108:109], s[6:7]
	v_mov_b64_e32 v[96:97], s[6:7]
	v_mov_b64_e32 v[92:93], s[6:7]
	v_mov_b64_e32 v[80:81], s[6:7]
	v_mov_b64_e32 v[72:73], s[6:7]
	v_mov_b64_e32 v[136:137], s[6:7]
	v_mov_b64_e32 v[132:133], s[6:7]
	v_mov_b64_e32 v[120:121], s[6:7]
	v_mov_b64_e32 v[116:117], s[6:7]
	v_mov_b64_e32 v[104:105], s[6:7]
	v_mov_b64_e32 v[100:101], s[6:7]
	v_mov_b64_e32 v[88:89], s[6:7]
	v_mov_b64_e32 v[84:85], s[6:7]
	v_mov_b64_e32 v[64:65], s[6:7]
	v_mov_b64_e32 v[60:61], s[6:7]
	v_mov_b64_e32 v[48:49], s[6:7]
	v_mov_b64_e32 v[44:45], s[6:7]
	v_mov_b64_e32 v[32:33], s[6:7]
	v_mov_b64_e32 v[28:29], s[6:7]
	v_mov_b64_e32 v[20:21], s[6:7]
	v_mov_b64_e32 v[16:17], s[6:7]
	v_mov_b64_e32 v[76:77], s[6:7]
	v_mov_b64_e32 v[68:69], s[6:7]
	v_mov_b64_e32 v[56:57], s[6:7]
	v_mov_b64_e32 v[52:53], s[6:7]
	v_mov_b64_e32 v[40:41], s[6:7]
	v_mov_b64_e32 v[36:37], s[6:7]
	v_mov_b64_e32 v[24:25], s[6:7]
	v_mov_b64_e32 v[10:11], s[4:5]
	v_mov_b64_e32 v[126:127], s[4:5]
	v_mov_b64_e32 v[122:123], s[4:5]
	v_mov_b64_e32 v[110:111], s[4:5]
	v_mov_b64_e32 v[106:107], s[4:5]
	v_mov_b64_e32 v[94:95], s[4:5]
	v_mov_b64_e32 v[90:91], s[4:5]
	v_mov_b64_e32 v[78:79], s[4:5]
	v_mov_b64_e32 v[70:71], s[4:5]
	v_mov_b64_e32 v[134:135], s[4:5]
	v_mov_b64_e32 v[130:131], s[4:5]
	v_mov_b64_e32 v[118:119], s[4:5]
	v_mov_b64_e32 v[114:115], s[4:5]
	v_mov_b64_e32 v[102:103], s[4:5]
	v_mov_b64_e32 v[98:99], s[4:5]
	v_mov_b64_e32 v[86:87], s[4:5]
	v_mov_b64_e32 v[82:83], s[4:5]
	v_mov_b64_e32 v[62:63], s[4:5]
	v_mov_b64_e32 v[58:59], s[4:5]
	v_mov_b64_e32 v[46:47], s[4:5]
	v_mov_b64_e32 v[42:43], s[4:5]
	v_mov_b64_e32 v[30:31], s[4:5]
	v_mov_b64_e32 v[26:27], s[4:5]
	v_mov_b64_e32 v[18:19], s[4:5]
	v_mov_b64_e32 v[14:15], s[4:5]
	v_mov_b64_e32 v[74:75], s[4:5]
	v_mov_b64_e32 v[66:67], s[4:5]
	v_mov_b64_e32 v[54:55], s[4:5]
	v_mov_b64_e32 v[50:51], s[4:5]
	v_mov_b64_e32 v[38:39], s[4:5]
	v_mov_b64_e32 v[34:35], s[4:5]
	v_mov_b64_e32 v[22:23], s[4:5]
	s_andn2_b64 vcc, exec, s[14:15]
	s_cbranch_vccnz .LBB0_1378
	s_barrier
	s_branch .LBB0_1378

; DI unsigned pk4_fp8(float a, float b, float c, float d) { unsigned p = 0u; p = __builtin_amdgcn_cvt_pk_fp8_f32(f8clamp(a), f8clamp(b), p, false); p = __builtin_amdgcn_cvt_pk_fp8_f32(f8clamp(c), f8clamp(d), p, true); return p; }
; DI float swiglu8(float xa, float xg) {
;     constexpr float sc = F8_HSC * F8_WSC, K1 = -1.4426950408889634f / sc, IK2 = sc * sc / F8_ASC;
;     const float e = __builtin_amdgcn_exp2f(xa * K1);
;     return (xa * xg) * __builtin_amdgcn_rcpf(__builtin_fmaf(e, IK2, IK2));
; }
;     DI void operator()(const pg8::f32x4 (&acc)[2][2][4][2], const pg8::Unit& u, int wr, int wc, int fr, int fq) const {
;         const int lpn = u.pn % nN; const int row0 = u.pm * 256 + wr * 64 + fr, col0 = lpn * 128 + wc * 32 + 8 * fq;
; #pragma unroll
;         for (int ai = 0; ai < 2; ++ai)
; #pragma unroll
;             for (int m = 0; m < 4; ++m) { unsigned char* p = act + (size_t)(row0 + ai * 128 + m * 16) * FF + col0;
;                 const pg8::f32x4 a0 = acc[ai][0][m][0], a1 = acc[ai][0][m][1], g0 = acc[ai][1][m][0], g1 = acc[ai][1][m][1];
;                 uint2 w; w.x = pk4_fp8(swiglu8(a0[0], g0[0]), swiglu8(a0[1], g0[1]), swiglu8(a0[2], g0[2]), swiglu8(a0[3], g0[3]));
;                 w.y = pk4_fp8(swiglu8(a1[0], g1[0]), swiglu8(a1[1], g1[1]), swiglu8(a1[2], g1[2]), swiglu8(a1[3], g1[3]));
;                 *(uint2*)p = w; }
;     }
.LBB0_2820:
	s_mov_b32 s84, 0xbb38aa3b
	s_mov_b32 s85, 0xbb38aa3b
	s_mov_b32 s86, 0x46800000
	s_mov_b32 s87, 0x46800000
	v_pk_mul_f32 v[134:135], v[134:135], v[126:127]
	v_pk_mul_f32 v[136:137], v[136:137], v[128:129]
	v_pk_mul_f32 v[130:131], v[130:131], v[122:123]
	v_pk_mul_f32 v[132:133], v[132:133], v[124:125]
	v_pk_mul_f32 v[126:127], v[126:127], s[84:85]
	v_pk_mul_f32 v[128:129], v[128:129], s[84:85]
	v_pk_mul_f32 v[122:123], v[122:123], s[84:85]
	v_pk_mul_f32 v[124:125], v[124:125], s[84:85]
	v_exp_f32_e32 v126, v126
	v_exp_f32_e32 v127, v127
	v_exp_f32_e32 v128, v128
	v_exp_f32_e32 v129, v129
	v_exp_f32_e32 v122, v122
	v_exp_f32_e32 v123, v123
	v_exp_f32_e32 v124, v124
	v_exp_f32_e32 v125, v125
	v_pk_fma_f32 v[126:127], v[126:127], s[86:87], v[170:171] op_sel:[0,0,1] op_sel_hi:[1,1,1]
	v_pk_fma_f32 v[128:129], v[128:129], s[86:87], v[170:171] op_sel:[0,0,1] op_sel_hi:[1,1,1]
	v_pk_fma_f32 v[122:123], v[122:123], s[86:87], v[170:171] op_sel:[0,0,1] op_sel_hi:[1,1,1]
	v_pk_fma_f32 v[124:125], v[124:125], s[86:87], v[170:171] op_sel:[0,0,1] op_sel_hi:[1,1,1]
	v_rcp_f32_e32 v126, v126
	v_rcp_f32_e32 v127, v127
	v_rcp_f32_e32 v128, v128
	v_rcp_f32_e32 v129, v129
	v_rcp_f32_e32 v122, v122
	v_rcp_f32_e32 v123, v123
	v_rcp_f32_e32 v124, v124
	v_rcp_f32_e32 v125, v125
	v_pk_mul_f32 v[134:135], v[134:135], v[126:127]
	v_pk_mul_f32 v[136:137], v[136:137], v[128:129]
	v_pk_mul_f32 v[130:131], v[130:131], v[122:123]
	v_pk_mul_f32 v[132:133], v[132:133], v[124:125]
	v_med3_f32 v134, v134, s51, v172
	v_med3_f32 v135, v135, s51, v172
	v_med3_f32 v136, v136, s51, v172
	v_med3_f32 v137, v137, s51, v172
	v_med3_f32 v130, v130, s51, v172
	v_med3_f32 v131, v131, s51, v172
	v_med3_f32 v132, v132, s51, v172
	v_med3_f32 v133, v133, s51, v172
	v_cvt_pk_fp8_f32 v126, v134, v135
	v_cvt_pk_fp8_f32 v126, v136, v137 op_sel:[0,0,1]
	v_cvt_pk_fp8_f32 v127, v130, v131
	v_cvt_pk_fp8_f32 v127, v132, v133 op_sel:[0,0,1]
	s_mul_hi_i32 s9, s59, 0x2e8ba2e9
	s_lshr_b32 s10, s9, 31
	s_lshr_b32 s9, s9, 2
	s_add_i32 s9, s9, s10
	s_mul_i32 s9, s9, 22
	s_sub_i32 s9, s59, s9
	v_lshl_add_u32 v6, s58, 8, v147
	v_lshl_or_b32 v2, s9, 7, v169
	v_mov_b64_e32 v[4:5], s[16:17]
	v_ashrrev_i32_e32 v3, 31, v2
	v_mad_i64_i32 v[122:123], s[10:11], v6, s49, v[4:5]
	v_lshl_add_u64 v[122:123], v[122:123], 0, v[2:3]
	global_store_dwordx2 v[122:123], v[126:127], off
	v_pk_mul_f32 v[118:119], v[118:119], v[110:111]
	v_pk_mul_f32 v[120:121], v[120:121], v[112:113]
	v_pk_mul_f32 v[114:115], v[114:115], v[106:107]
	v_pk_mul_f32 v[116:117], v[116:117], v[108:109]
	v_pk_mul_f32 v[110:111], v[110:111], s[84:85]
	v_pk_mul_f32 v[112:113], v[112:113], s[84:85]
	v_pk_mul_f32 v[106:107], v[106:107], s[84:85]
	v_pk_mul_f32 v[108:109], v[108:109], s[84:85]
	v_exp_f32_e32 v110, v110
	v_exp_f32_e32 v111, v111
	v_exp_f32_e32 v112, v112
	v_exp_f32_e32 v113, v113
	v_exp_f32_e32 v106, v106
	v_exp_f32_e32 v107, v107
	v_exp_f32_e32 v108, v108
	v_exp_f32_e32 v109, v109
	v_pk_fma_f32 v[110:111], v[110:111], s[86:87], v[170:171] op_sel:[0,0,1] op_sel_hi:[1,1,1]
	v_pk_fma_f32 v[112:113], v[112:113], s[86:87], v[170:171] op_sel:[0,0,1] op_sel_hi:[1,1,1]
	v_pk_fma_f32 v[106:107], v[106:107], s[86:87], v[170:171] op_sel:[0,0,1] op_sel_hi:[1,1,1]
	v_pk_fma_f32 v[108:109], v[108:109], s[86:87], v[170:171] op_sel:[0,0,1] op_sel_hi:[1,1,1]
	v_rcp_f32_e32 v110, v110
	v_rcp_f32_e32 v111, v111
	v_rcp_f32_e32 v112, v112
	v_rcp_f32_e32 v113, v113
	v_rcp_f32_e32 v106, v106
	v_rcp_f32_e32 v107, v107
	v_rcp_f32_e32 v108, v108
	v_rcp_f32_e32 v109, v109
	v_pk_mul_f32 v[118:119], v[118:119], v[110:111]
	v_pk_mul_f32 v[120:121], v[120:121], v[112:113]
	v_pk_mul_f32 v[114:115], v[114:115], v[106:107]
	v_pk_mul_f32 v[116:117], v[116:117], v[108:109]
	v_med3_f32 v118, v118, s51, v172
	v_med3_f32 v119, v119, s51, v172
	v_med3_f32 v120, v120, s51, v172
	v_med3_f32 v121, v121, s51, v172
	v_med3_f32 v114, v114, s51, v172
	v_med3_f32 v115, v115, s51, v172
	v_med3_f32 v116, v116, s51, v172
	v_med3_f32 v117, v117, s51, v172
	v_cvt_pk_fp8_f32 v110, v118, v119
	v_cvt_pk_fp8_f32 v110, v120, v121 op_sel:[0,0,1]
	v_cvt_pk_fp8_f32 v111, v114, v115
	v_cvt_pk_fp8_f32 v111, v116, v117 op_sel:[0,0,1]
	v_or_b32_e32 v7, 16, v6
	v_mad_i64_i32 v[106:107], s[10:11], v7, s49, v[4:5]
	v_lshl_add_u64 v[106:107], v[106:107], 0, v[2:3]
	global_store_dwordx2 v[106:107], v[110:111], off
	v_pk_mul_f32 v[102:103], v[102:103], v[94:95]
	v_pk_mul_f32 v[104:105], v[104:105], v[96:97]
	v_pk_mul_f32 v[98:99], v[98:99], v[90:91]
	v_pk_mul_f32 v[100:101], v[100:101], v[92:93]
	v_pk_mul_f32 v[94:95], v[94:95], s[84:85]
	v_pk_mul_f32 v[96:97], v[96:97], s[84:85]
	v_pk_mul_f32 v[90:91], v[90:91], s[84:85]
	v_pk_mul_f32 v[92:93], v[92:93], s[84:85]
	v_exp_f32_e32 v94, v94
	v_exp_f32_e32 v95, v95
	v_exp_f32_e32 v96, v96
	v_exp_f32_e32 v97, v97
	v_exp_f32_e32 v90, v90
	v_exp_f32_e32 v91, v91
	v_exp_f32_e32 v92, v92
	v_exp_f32_e32 v93, v93
	v_pk_fma_f32 v[94:95], v[94:95], s[86:87], v[170:171] op_sel:[0,0,1] op_sel_hi:[1,1,1]
	v_pk_fma_f32 v[96:97], v[96:97], s[86:87], v[170:171] op_sel:[0,0,1] op_sel_hi:[1,1,1]
	v_pk_fma_f32 v[90:91], v[90:91], s[86:87], v[170:171] op_sel:[0,0,1] op_sel_hi:[1,1,1]
	v_pk_fma_f32 v[92:93], v[92:93], s[86:87], v[170:171] op_sel:[0,0,1] op_sel_hi:[1,1,1]
	v_rcp_f32_e32 v94, v94
	v_rcp_f32_e32 v95, v95
	v_rcp_f32_e32 v96, v96
	v_rcp_f32_e32 v97, v97
	v_rcp_f32_e32 v90, v90
	v_rcp_f32_e32 v91, v91
	v_rcp_f32_e32 v92, v92
	v_rcp_f32_e32 v93, v93
	v_pk_mul_f32 v[102:103], v[102:103], v[94:95]
	v_pk_mul_f32 v[104:105], v[104:105], v[96:97]
	v_pk_mul_f32 v[98:99], v[98:99], v[90:91]
	v_pk_mul_f32 v[100:101], v[100:101], v[92:93]
	v_med3_f32 v102, v102, s51, v172
; DI unsigned pk4_fp8(float a, float b, float c, float d) { unsigned p = 0u; p = __builtin_amdgcn_cvt_pk_fp8_f32(f8clamp(a), f8clamp(b), p, false); p = __builtin_amdgcn_cvt_pk_fp8_f32(f8clamp(c), f8clamp(d), p, true); return p; }
; DI float swiglu8(float xa, float xg) {
;     constexpr float sc = F8_HSC * F8_WSC, K1 = -1.4426950408889634f / sc, IK2 = sc * sc / F8_ASC;
;     const float e = __builtin_amdgcn_exp2f(xa * K1);
;     return (xa * xg) * __builtin_amdgcn_rcpf(__builtin_fmaf(e, IK2, IK2));
; }
;     DI void operator()(const pg8::f32x4 (&acc)[2][2][4][2], const pg8::Unit& u, int wr, int wc, int fr, int fq) const {
;         const int lpn = u.pn % nN; const int row0 = u.pm * 256 + wr * 64 + fr, col0 = lpn * 128 + wc * 32 + 8 * fq;
; #pragma unroll
;         for (int ai = 0; ai < 2; ++ai)
; #pragma unroll
;             for (int m = 0; m < 4; ++m) { unsigned char* p = act + (size_t)(row0 + ai * 128 + m * 16) * FF + col0;
;                 const pg8::f32x4 a0 = acc[ai][0][m][0], a1 = acc[ai][0][m][1], g0 = acc[ai][1][m][0], g1 = acc[ai][1][m][1];
;                 uint2 w; w.x = pk4_fp8(swiglu8(a0[0], g0[0]), swiglu8(a0[1], g0[1]), swiglu8(a0[2], g0[2]), swiglu8(a0[3], g0[3]));
;                 w.y = pk4_fp8(swiglu8(a1[0], g1[0]), swiglu8(a1[1], g1[1]), swiglu8(a1[2], g1[2]), swiglu8(a1[3], g1[3]));
;                 *(uint2*)p = w; }
	v_med3_f32 v103, v103, s51, v172
	v_med3_f32 v104, v104, s51, v172
	v_med3_f32 v105, v105, s51, v172
	v_med3_f32 v98, v98, s51, v172
	v_med3_f32 v99, v99, s51, v172
	v_med3_f32 v100, v100, s51, v172
	v_med3_f32 v101, v101, s51, v172
	v_cvt_pk_fp8_f32 v94, v102, v103
	v_cvt_pk_fp8_f32 v94, v104, v105 op_sel:[0,0,1]
	v_cvt_pk_fp8_f32 v95, v98, v99
	v_cvt_pk_fp8_f32 v95, v100, v101 op_sel:[0,0,1]
	v_or_b32_e32 v7, 32, v6
	v_mad_i64_i32 v[90:91], s[10:11], v7, s49, v[4:5]
	v_lshl_add_u64 v[90:91], v[90:91], 0, v[2:3]
	global_store_dwordx2 v[90:91], v[94:95], off
	v_pk_mul_f32 v[86:87], v[86:87], v[78:79]
	v_pk_mul_f32 v[88:89], v[88:89], v[80:81]
	v_pk_mul_f32 v[82:83], v[82:83], v[70:71]
	v_pk_mul_f32 v[84:85], v[84:85], v[72:73]
	v_pk_mul_f32 v[78:79], v[78:79], s[84:85]
	v_pk_mul_f32 v[80:81], v[80:81], s[84:85]
	v_pk_mul_f32 v[70:71], v[70:71], s[84:85]
	v_pk_mul_f32 v[72:73], v[72:73], s[84:85]
	v_exp_f32_e32 v78, v78
	v_exp_f32_e32 v79, v79
	v_exp_f32_e32 v80, v80
	v_exp_f32_e32 v81, v81
	v_exp_f32_e32 v70, v70
	v_exp_f32_e32 v71, v71
	v_exp_f32_e32 v72, v72
	v_exp_f32_e32 v73, v73
	v_pk_fma_f32 v[78:79], v[78:79], s[86:87], v[170:171] op_sel:[0,0,1] op_sel_hi:[1,1,1]
	v_pk_fma_f32 v[80:81], v[80:81], s[86:87], v[170:171] op_sel:[0,0,1] op_sel_hi:[1,1,1]
	v_pk_fma_f32 v[70:71], v[70:71], s[86:87], v[170:171] op_sel:[0,0,1] op_sel_hi:[1,1,1]
	v_pk_fma_f32 v[72:73], v[72:73], s[86:87], v[170:171] op_sel:[0,0,1] op_sel_hi:[1,1,1]
	v_rcp_f32_e32 v78, v78
	v_rcp_f32_e32 v79, v79
	v_rcp_f32_e32 v80, v80
	v_rcp_f32_e32 v81, v81
	v_rcp_f32_e32 v70, v70
	v_rcp_f32_e32 v71, v71
	v_rcp_f32_e32 v72, v72
	v_rcp_f32_e32 v73, v73
	v_pk_mul_f32 v[86:87], v[86:87], v[78:79]
	v_pk_mul_f32 v[88:89], v[88:89], v[80:81]
	v_pk_mul_f32 v[82:83], v[82:83], v[70:71]
	v_pk_mul_f32 v[84:85], v[84:85], v[72:73]
	v_med3_f32 v86, v86, s51, v172
	v_med3_f32 v87, v87, s51, v172
	v_med3_f32 v88, v88, s51, v172
	v_med3_f32 v89, v89, s51, v172
	v_med3_f32 v82, v82, s51, v172
	v_med3_f32 v83, v83, s51, v172
	v_med3_f32 v84, v84, s51, v172
	v_med3_f32 v85, v85, s51, v172
	v_cvt_pk_fp8_f32 v78, v86, v87
	v_cvt_pk_fp8_f32 v78, v88, v89 op_sel:[0,0,1]
	v_cvt_pk_fp8_f32 v79, v82, v83
	v_cvt_pk_fp8_f32 v79, v84, v85 op_sel:[0,0,1]
	v_or_b32_e32 v7, 48, v6
	v_mad_i64_i32 v[70:71], s[10:11], v7, s49, v[4:5]
	v_lshl_add_u64 v[70:71], v[70:71], 0, v[2:3]
	global_store_dwordx2 v[70:71], v[78:79], off
	v_pk_mul_f32 v[74:75], v[74:75], v[62:63]
	v_pk_mul_f32 v[76:77], v[76:77], v[64:65]
	v_pk_mul_f32 v[66:67], v[66:67], v[58:59]
	v_pk_mul_f32 v[68:69], v[68:69], v[60:61]
	v_pk_mul_f32 v[62:63], v[62:63], s[84:85]
	v_pk_mul_f32 v[64:65], v[64:65], s[84:85]
	v_pk_mul_f32 v[58:59], v[58:59], s[84:85]
	v_pk_mul_f32 v[60:61], v[60:61], s[84:85]
	v_exp_f32_e32 v62, v62
	v_exp_f32_e32 v63, v63
	v_exp_f32_e32 v64, v64
	v_exp_f32_e32 v65, v65
	v_exp_f32_e32 v58, v58
	v_exp_f32_e32 v59, v59
	v_exp_f32_e32 v60, v60
	v_exp_f32_e32 v61, v61
	v_pk_fma_f32 v[62:63], v[62:63], s[86:87], v[170:171] op_sel:[0,0,1] op_sel_hi:[1,1,1]
	v_pk_fma_f32 v[64:65], v[64:65], s[86:87], v[170:171] op_sel:[0,0,1] op_sel_hi:[1,1,1]
	v_pk_fma_f32 v[58:59], v[58:59], s[86:87], v[170:171] op_sel:[0,0,1] op_sel_hi:[1,1,1]
	v_pk_fma_f32 v[60:61], v[60:61], s[86:87], v[170:171] op_sel:[0,0,1] op_sel_hi:[1,1,1]
	v_rcp_f32_e32 v62, v62
	v_rcp_f32_e32 v63, v63
	v_rcp_f32_e32 v64, v64
	v_rcp_f32_e32 v65, v65
	v_rcp_f32_e32 v58, v58
	v_rcp_f32_e32 v59, v59
	v_rcp_f32_e32 v60, v60
	v_rcp_f32_e32 v61, v61
	v_pk_mul_f32 v[74:75], v[74:75], v[62:63]
	v_pk_mul_f32 v[76:77], v[76:77], v[64:65]
	v_pk_mul_f32 v[66:67], v[66:67], v[58:59]
	v_pk_mul_f32 v[68:69], v[68:69], v[60:61]
	v_med3_f32 v74, v74, s51, v172
	v_med3_f32 v75, v75, s51, v172
	v_med3_f32 v76, v76, s51, v172
	v_med3_f32 v77, v77, s51, v172
	v_med3_f32 v66, v66, s51, v172
	v_med3_f32 v67, v67, s51, v172
	v_med3_f32 v68, v68, s51, v172
	v_med3_f32 v69, v69, s51, v172
	v_cvt_pk_fp8_f32 v62, v74, v75
	v_cvt_pk_fp8_f32 v62, v76, v77 op_sel:[0,0,1]
	v_cvt_pk_fp8_f32 v63, v66, v67
	v_cvt_pk_fp8_f32 v63, v68, v69 op_sel:[0,0,1]
	v_add_u32_e32 v7, 0x80, v6
	v_mad_i64_i32 v[58:59], s[10:11], v7, s49, v[4:5]
	v_lshl_add_u64 v[58:59], v[58:59], 0, v[2:3]
	global_store_dwordx2 v[58:59], v[62:63], off
	v_pk_mul_f32 v[54:55], v[54:55], v[46:47]
	v_pk_mul_f32 v[56:57], v[56:57], v[48:49]
	v_pk_mul_f32 v[50:51], v[50:51], v[42:43]
	v_pk_mul_f32 v[52:53], v[52:53], v[44:45]
	v_pk_mul_f32 v[46:47], v[46:47], s[84:85]
	v_pk_mul_f32 v[48:49], v[48:49], s[84:85]
	v_pk_mul_f32 v[42:43], v[42:43], s[84:85]
	v_pk_mul_f32 v[44:45], v[44:45], s[84:85]
	v_exp_f32_e32 v46, v46
	v_exp_f32_e32 v47, v47
	v_exp_f32_e32 v48, v48
	v_exp_f32_e32 v49, v49
	v_exp_f32_e32 v42, v42
	v_exp_f32_e32 v43, v43
	v_exp_f32_e32 v44, v44
	v_exp_f32_e32 v45, v45
	v_pk_fma_f32 v[46:47], v[46:47], s[86:87], v[170:171] op_sel:[0,0,1] op_sel_hi:[1,1,1]
	v_pk_fma_f32 v[48:49], v[48:49], s[86:87], v[170:171] op_sel:[0,0,1] op_sel_hi:[1,1,1]
	v_pk_fma_f32 v[42:43], v[42:43], s[86:87], v[170:171] op_sel:[0,0,1] op_sel_hi:[1,1,1]
	v_pk_fma_f32 v[44:45], v[44:45], s[86:87], v[170:171] op_sel:[0,0,1] op_sel_hi:[1,1,1]
	v_rcp_f32_e32 v46, v46
	v_rcp_f32_e32 v47, v47
	v_rcp_f32_e32 v48, v48
	v_rcp_f32_e32 v49, v49
	v_rcp_f32_e32 v42, v42
	v_rcp_f32_e32 v43, v43
	v_rcp_f32_e32 v44, v44
	v_rcp_f32_e32 v45, v45
	v_pk_mul_f32 v[54:55], v[54:55], v[46:47]
	v_pk_mul_f32 v[56:57], v[56:57], v[48:49]
	v_pk_mul_f32 v[50:51], v[50:51], v[42:43]
	v_pk_mul_f32 v[52:53], v[52:53], v[44:45]
	v_med3_f32 v54, v54, s51, v172
	v_med3_f32 v55, v55, s51, v172
	v_med3_f32 v56, v56, s51, v172
	v_med3_f32 v57, v57, s51, v172
	v_med3_f32 v50, v50, s51, v172
; #define PG8_BAR __builtin_amdgcn_s_barrier()
; DI unsigned pk4_fp8(float a, float b, float c, float d) { unsigned p = 0u; p = __builtin_amdgcn_cvt_pk_fp8_f32(f8clamp(a), f8clamp(b), p, false); p = __builtin_amdgcn_cvt_pk_fp8_f32(f8clamp(c), f8clamp(d), p, true); return p; }
; template <class Epi, class Sched, bool ALIGN_EPI = false, bool SP2 = false, bool F8 = false>
; __device__ __forceinline__ void gemm_phase(PG8_LAS unsigned char* lds, const Gemm g, const Sched& S, const Epi& E) {
;     ...
;         if (!has_next) break;
; #pragma unroll
;         for (int a = 0; a < 2; ++a)
; #pragma unroll
;             for (int b = 0; b < 2; ++b)
; #pragma unroll
;                 for (int m = 0; m < 4; ++m)
; #pragma unroll
;                     for (int n = 0; n < 2; ++n) { acc[a][b][m][n] = (f32x4){0.f, 0.f, 0.f, 0.f}; if constexpr (F8) asm volatile("" : "+v"(acc[a][b][m][n])); }
;         cur = nxt; cA = nA; cB = nB; ++ui;
;         if constexpr (ALIGN_EPI) { if (wr == 1) PG8_BAR; }
; DI float swiglu8(float xa, float xg) {
;     constexpr float sc = F8_HSC * F8_WSC, K1 = -1.4426950408889634f / sc, IK2 = sc * sc / F8_ASC;
;     const float e = __builtin_amdgcn_exp2f(xa * K1);
;     return (xa * xg) * __builtin_amdgcn_rcpf(__builtin_fmaf(e, IK2, IK2));
; }
;     DI void operator()(const pg8::f32x4 (&acc)[2][2][4][2], const pg8::Unit& u, int wr, int wc, int fr, int fq) const {
;         const int lpn = u.pn % nN; const int row0 = u.pm * 256 + wr * 64 + fr, col0 = lpn * 128 + wc * 32 + 8 * fq;
; #pragma unroll
;         for (int ai = 0; ai < 2; ++ai)
; #pragma unroll
;             for (int m = 0; m < 4; ++m) { unsigned char* p = act + (size_t)(row0 + ai * 128 + m * 16) * FF + col0;
;                 const pg8::f32x4 a0 = acc[ai][0][m][0], a1 = acc[ai][0][m][1], g0 = acc[ai][1][m][0], g1 = acc[ai][1][m][1];
;                 uint2 w; w.x = pk4_fp8(swiglu8(a0[0], g0[0]), swiglu8(a0[1], g0[1]), swiglu8(a0[2], g0[2]), swiglu8(a0[3], g0[3]));
;                 w.y = pk4_fp8(swiglu8(a1[0], g1[0]), swiglu8(a1[1], g1[1]), swiglu8(a1[2], g1[2]), swiglu8(a1[3], g1[3]));
;                 *(uint2*)p = w; }
	v_med3_f32 v51, v51, s51, v172
	v_med3_f32 v52, v52, s51, v172
	v_med3_f32 v53, v53, s51, v172
	v_cvt_pk_fp8_f32 v46, v54, v55
	v_cvt_pk_fp8_f32 v46, v56, v57 op_sel:[0,0,1]
	v_cvt_pk_fp8_f32 v47, v50, v51
	v_cvt_pk_fp8_f32 v47, v52, v53 op_sel:[0,0,1]
	v_add_u32_e32 v7, 0x90, v6
	v_mad_i64_i32 v[42:43], s[10:11], v7, s49, v[4:5]
	v_lshl_add_u64 v[42:43], v[42:43], 0, v[2:3]
	global_store_dwordx2 v[42:43], v[46:47], off
	v_pk_mul_f32 v[38:39], v[38:39], v[30:31]
	v_pk_mul_f32 v[40:41], v[40:41], v[32:33]
	v_pk_mul_f32 v[34:35], v[34:35], v[26:27]
	v_pk_mul_f32 v[36:37], v[36:37], v[28:29]
	v_pk_mul_f32 v[30:31], v[30:31], s[84:85]
	v_pk_mul_f32 v[32:33], v[32:33], s[84:85]
	v_pk_mul_f32 v[26:27], v[26:27], s[84:85]
	v_pk_mul_f32 v[28:29], v[28:29], s[84:85]
	v_exp_f32_e32 v30, v30
	v_exp_f32_e32 v31, v31
	v_exp_f32_e32 v32, v32
	v_exp_f32_e32 v33, v33
	v_exp_f32_e32 v26, v26
	v_exp_f32_e32 v27, v27
	v_exp_f32_e32 v28, v28
	v_exp_f32_e32 v29, v29
	v_pk_fma_f32 v[30:31], v[30:31], s[86:87], v[170:171] op_sel:[0,0,1] op_sel_hi:[1,1,1]
	v_pk_fma_f32 v[32:33], v[32:33], s[86:87], v[170:171] op_sel:[0,0,1] op_sel_hi:[1,1,1]
	v_pk_fma_f32 v[26:27], v[26:27], s[86:87], v[170:171] op_sel:[0,0,1] op_sel_hi:[1,1,1]
	v_pk_fma_f32 v[28:29], v[28:29], s[86:87], v[170:171] op_sel:[0,0,1] op_sel_hi:[1,1,1]
	v_rcp_f32_e32 v30, v30
	v_rcp_f32_e32 v31, v31
	v_rcp_f32_e32 v32, v32
	v_rcp_f32_e32 v33, v33
	v_rcp_f32_e32 v26, v26
	v_rcp_f32_e32 v27, v27
	v_rcp_f32_e32 v28, v28
	v_rcp_f32_e32 v29, v29
	v_pk_mul_f32 v[38:39], v[38:39], v[30:31]
	v_pk_mul_f32 v[40:41], v[40:41], v[32:33]
	v_pk_mul_f32 v[34:35], v[34:35], v[26:27]
	v_pk_mul_f32 v[36:37], v[36:37], v[28:29]
	v_med3_f32 v38, v38, s51, v172
	v_med3_f32 v39, v39, s51, v172
	v_med3_f32 v40, v40, s51, v172
	v_med3_f32 v41, v41, s51, v172
	v_med3_f32 v34, v34, s51, v172
	v_med3_f32 v35, v35, s51, v172
	v_med3_f32 v36, v36, s51, v172
	v_med3_f32 v37, v37, s51, v172
	v_cvt_pk_fp8_f32 v30, v38, v39
	v_cvt_pk_fp8_f32 v30, v40, v41 op_sel:[0,0,1]
	v_cvt_pk_fp8_f32 v31, v34, v35
	v_cvt_pk_fp8_f32 v31, v36, v37 op_sel:[0,0,1]
	v_add_u32_e32 v7, 0xa0, v6
	v_mad_i64_i32 v[26:27], s[10:11], v7, s49, v[4:5]
	v_lshl_add_u64 v[26:27], v[26:27], 0, v[2:3]
	global_store_dwordx2 v[26:27], v[30:31], off
	v_pk_mul_f32 v[22:23], v[22:23], v[18:19]
	v_pk_mul_f32 v[24:25], v[24:25], v[20:21]
	v_pk_mul_f32 v[10:11], v[10:11], v[14:15]
	v_pk_mul_f32 v[12:13], v[12:13], v[16:17]
	v_pk_mul_f32 v[18:19], v[18:19], s[84:85]
	v_pk_mul_f32 v[20:21], v[20:21], s[84:85]
	v_pk_mul_f32 v[14:15], v[14:15], s[84:85]
	v_pk_mul_f32 v[16:17], v[16:17], s[84:85]
	v_exp_f32_e32 v18, v18
	v_exp_f32_e32 v19, v19
	v_exp_f32_e32 v20, v20
	v_exp_f32_e32 v21, v21
	v_exp_f32_e32 v14, v14
	v_exp_f32_e32 v15, v15
	v_exp_f32_e32 v16, v16
	v_exp_f32_e32 v17, v17
	v_pk_fma_f32 v[18:19], v[18:19], s[86:87], v[170:171] op_sel:[0,0,1] op_sel_hi:[1,1,1]
	v_pk_fma_f32 v[20:21], v[20:21], s[86:87], v[170:171] op_sel:[0,0,1] op_sel_hi:[1,1,1]
	v_pk_fma_f32 v[14:15], v[14:15], s[86:87], v[170:171] op_sel:[0,0,1] op_sel_hi:[1,1,1]
	v_pk_fma_f32 v[16:17], v[16:17], s[86:87], v[170:171] op_sel:[0,0,1] op_sel_hi:[1,1,1]
	v_rcp_f32_e32 v18, v18
	v_rcp_f32_e32 v19, v19
	v_rcp_f32_e32 v20, v20
	v_rcp_f32_e32 v21, v21
	v_rcp_f32_e32 v14, v14
	v_rcp_f32_e32 v15, v15
	v_rcp_f32_e32 v16, v16
	v_rcp_f32_e32 v17, v17
	v_pk_mul_f32 v[22:23], v[22:23], v[18:19]
	v_pk_mul_f32 v[24:25], v[24:25], v[20:21]
	v_pk_mul_f32 v[10:11], v[10:11], v[14:15]
	v_pk_mul_f32 v[12:13], v[12:13], v[16:17]
	v_med3_f32 v22, v22, s51, v172
	v_med3_f32 v23, v23, s51, v172
	v_med3_f32 v24, v24, s51, v172
	v_med3_f32 v25, v25, s51, v172
	v_med3_f32 v10, v10, s51, v172
	v_med3_f32 v11, v11, s51, v172
	v_med3_f32 v12, v12, s51, v172
	v_med3_f32 v13, v13, s51, v172
	v_cvt_pk_fp8_f32 v18, v22, v23
	v_cvt_pk_fp8_f32 v18, v24, v25 op_sel:[0,0,1]
	v_cvt_pk_fp8_f32 v19, v10, v11
	v_cvt_pk_fp8_f32 v19, v12, v13 op_sel:[0,0,1]
	v_add_u32_e32 v8, 0xb0, v6
	v_mad_i64_i32 v[4:5], s[10:11], v8, s49, v[4:5]
	v_lshl_add_u64 v[2:3], v[4:5], 0, v[2:3]
	s_and_b64 vcc, exec, s[0:1]
	s_mov_b64 s[0:1], -1
	global_store_dwordx2 v[2:3], v[18:19], off
	s_cbranch_vccnz .LBB0_2808
	s_mov_b32 s10, s8
	s_mov_b32 s11, s8
	s_mov_b32 s9, s8
	v_mov_b64_e32 v[12:13], s[10:11]
	v_mov_b64_e32 v[128:129], s[10:11]
	v_mov_b64_e32 v[124:125], s[10:11]
	v_mov_b64_e32 v[112:113], s[10:11]
	v_mov_b64_e32 v[108:109], s[10:11]
	v_mov_b64_e32 v[96:97], s[10:11]
	v_mov_b64_e32 v[92:93], s[10:11]
	v_mov_b64_e32 v[80:81], s[10:11]
	v_mov_b64_e32 v[72:73], s[10:11]
	v_mov_b64_e32 v[136:137], s[10:11]
	v_mov_b64_e32 v[132:133], s[10:11]
	v_mov_b64_e32 v[120:121], s[10:11]
	v_mov_b64_e32 v[116:117], s[10:11]
	v_mov_b64_e32 v[104:105], s[10:11]
	v_mov_b64_e32 v[100:101], s[10:11]
	v_mov_b64_e32 v[88:89], s[10:11]
	v_mov_b64_e32 v[84:85], s[10:11]
	v_mov_b64_e32 v[64:65], s[10:11]
	v_mov_b64_e32 v[60:61], s[10:11]
	v_mov_b64_e32 v[48:49], s[10:11]
	v_mov_b64_e32 v[44:45], s[10:11]
	v_mov_b64_e32 v[32:33], s[10:11]
	v_mov_b64_e32 v[28:29], s[10:11]
	v_mov_b64_e32 v[20:21], s[10:11]
	v_mov_b64_e32 v[16:17], s[10:11]
	v_mov_b64_e32 v[76:77], s[10:11]
	v_mov_b64_e32 v[68:69], s[10:11]
	v_mov_b64_e32 v[56:57], s[10:11]
	v_mov_b64_e32 v[52:53], s[10:11]
	v_mov_b64_e32 v[40:41], s[10:11]
	v_mov_b64_e32 v[36:37], s[10:11]
	v_mov_b64_e32 v[24:25], s[10:11]
	v_mov_b64_e32 v[10:11], s[8:9]
	v_mov_b64_e32 v[126:127], s[8:9]
	v_mov_b64_e32 v[122:123], s[8:9]
	v_mov_b64_e32 v[110:111], s[8:9]
	v_mov_b64_e32 v[106:107], s[8:9]
	v_mov_b64_e32 v[94:95], s[8:9]
	v_mov_b64_e32 v[90:91], s[8:9]
	v_mov_b64_e32 v[78:79], s[8:9]
	v_mov_b64_e32 v[70:71], s[8:9]
	v_mov_b64_e32 v[134:135], s[8:9]
	v_mov_b64_e32 v[130:131], s[8:9]
	v_mov_b64_e32 v[118:119], s[8:9]
	v_mov_b64_e32 v[114:115], s[8:9]
	v_mov_b64_e32 v[102:103], s[8:9]
	v_mov_b64_e32 v[98:99], s[8:9]
	v_mov_b64_e32 v[86:87], s[8:9]
	v_mov_b64_e32 v[82:83], s[8:9]
	v_mov_b64_e32 v[62:63], s[8:9]
	v_mov_b64_e32 v[58:59], s[8:9]
	v_mov_b64_e32 v[46:47], s[8:9]
	v_mov_b64_e32 v[42:43], s[8:9]
	v_mov_b64_e32 v[30:31], s[8:9]
	v_mov_b64_e32 v[26:27], s[8:9]
	v_mov_b64_e32 v[18:19], s[8:9]
	v_mov_b64_e32 v[14:15], s[8:9]
	v_mov_b64_e32 v[74:75], s[8:9]
	v_mov_b64_e32 v[66:67], s[8:9]
	v_mov_b64_e32 v[54:55], s[8:9]
	v_mov_b64_e32 v[50:51], s[8:9]
	v_mov_b64_e32 v[38:39], s[8:9]
	v_mov_b64_e32 v[34:35], s[8:9]
	v_mov_b64_e32 v[22:23], s[8:9]
	s_andn2_b64 vcc, exec, s[14:15]
	s_cbranch_vccnz .LBB0_2807
	s_barrier
	s_branch .LBB0_2807
